# grid barrier: leader L2 invalidate overlapped with top-level arrival, no wait after generation bump, non-leader L1 invalidate before polling
# speedup vs baseline: 1.0002x; 1.0002x over previous
; __device__ __forceinline__ unsigned xb_ld(unsigned* p)              { return __hip_atomic_load(p, __ATOMIC_RELAXED, __HIP_MEMORY_SCOPE_AGENT); }
; __device__ __forceinline__ unsigned xb_add(unsigned* p, unsigned v) { return __hip_atomic_fetch_add(p, v, __ATOMIC_RELAXED, __HIP_MEMORY_SCOPE_AGENT); }
; #define XB_SPIN(cond, bar) do { unsigned _sp = 0; while (cond) { __builtin_amdgcn_s_sleep(1); \
;     if ((++_sp & 255u) == 0u) { if (xb_ld(&(bar)[XB_TMO])) break; if (_sp > XB_SPIN_CAP) { atomicAdd(&(bar)[XB_TMO], 1u); break; } } } } while (0)
;     __device__ __forceinline__ const float* x() const { return (const float*)ld(0); }
; __device__ __forceinline__ void xcd_barrier(const XcdBarrier& b) {
;     ...
;     if (threadIdx.x == 0) {
;         unsigned* bar = b.bar;
;         __builtin_amdgcn_s_waitcnt(0);
;         unsigned nloc = b.st[0], nx = b.st[1];
;         if (nloc == 0u) { xcd_barrier_complete(bar, b.x, nloc, nx); b.st[0] = nloc; b.st[1] = nx; }
;         const unsigned old = xb_add(&bar[XB_XSUB(b.x)], 1u);
;         const unsigned gen = old / nloc;
;         if (old + 1u == (gen + 1u) * nloc) {
;             __builtin_amdgcn_fence(__ATOMIC_RELEASE, "agent");
;             asm volatile("s_waitcnt vmcnt(0)" ::: "memory");
;             const unsigned og = xb_add(&bar[XB_TOP], 1u);
;             const unsigned tg = og / nx;
;             if (og + 1u == (tg + 1u) * nx) xb_add(&bar[XB_TOPGEN], 1u);
;             else XB_SPIN(xb_ld(&bar[XB_TOPGEN]) == tg, bar);
;             __builtin_amdgcn_fence(__ATOMIC_ACQUIRE, "agent");
;             asm volatile("s_waitcnt vmcnt(0)" ::: "memory");
;             xb_add(&bar[XB_XGEN(b.x)], 1u);
;             asm volatile("s_waitcnt vmcnt(0)" ::: "memory");
;         } else {
;             XB_SPIN(xb_ld(&bar[XB_XGEN(b.x)]) == gen, bar);
;             asm volatile("buffer_inv sc0\n\ts_waitcnt vmcnt(0)" ::: "memory");
.LBB0_185:
	v_readlane_b32 s2, v248, 2
	s_lshl_b32 s2, s2, 8
	s_add_u32 s6, s92, s2
	s_addc_u32 s7, s93, 0
	v_mov_b32_e32 v2, 0x1000
	v_mov_b32_e32 v4, 1
	global_atomic_add v4, v2, v4, s[6:7] offset:1024 sc0
	v_cvt_f32_u32_e32 v2, v3
	v_sub_u32_e32 v5, 0, v3
	v_rcp_iflag_f32_e32 v2, v2
	s_nop 0
	v_mul_f32_e32 v2, 0x4f7ffffe, v2
	v_cvt_u32_f32_e32 v2, v2
	v_mul_lo_u32 v5, v5, v2
	v_mul_hi_u32 v5, v2, v5
	v_add_u32_e32 v2, v2, v5
	s_waitcnt vmcnt(0)
	v_mul_hi_u32 v2, v4, v2
	v_mul_lo_u32 v5, v2, v3
	v_sub_u32_e32 v5, v4, v5
	v_add_u32_e32 v6, 1, v2
	v_cmp_ge_u32_e32 vcc, v5, v3
	v_add_u32_e32 v4, 1, v4
	s_nop 0
	v_cndmask_b32_e32 v2, v2, v6, vcc
	v_sub_u32_e32 v6, v5, v3
	v_cndmask_b32_e32 v5, v5, v6, vcc
	v_add_u32_e32 v6, 1, v2
	v_cmp_ge_u32_e32 vcc, v5, v3
	s_nop 1
	v_cndmask_b32_e32 v2, v2, v6, vcc
	v_mul_lo_u32 v5, v3, v2
	v_add_u32_e32 v3, v5, v3
	v_cmp_ne_u32_e32 vcc, v4, v3
	s_and_saveexec_b64 s[2:3], vcc
	s_xor_b64 s[2:3], exec, s[2:3]
	s_cbranch_execz .LBB0_199
	s_waitcnt lgkmcnt(0)
	buffer_inv sc0
	v_mov_b32_e32 v1, 0x2000
	global_load_dword v1, v1, s[6:7] offset:1024 sc1
	s_add_u32 s10, s6, 0x2400
	s_addc_u32 s11, s7, 0
	s_waitcnt vmcnt(0)
	v_cmp_eq_u32_e32 vcc, v1, v2
	s_and_saveexec_b64 s[8:9], vcc
	s_cbranch_execz .LBB0_198
	s_mov_b32 s22, 1
	s_mov_b64 s[12:13], 0
	v_mov_b32_e32 v1, 0
	s_branch .LBB0_189

; __device__ __forceinline__ unsigned xb_ld(unsigned* p)              { return __hip_atomic_load(p, __ATOMIC_RELAXED, __HIP_MEMORY_SCOPE_AGENT); }
; #define XB_SPIN(cond, bar) do { unsigned _sp = 0; while (cond) { __builtin_amdgcn_s_sleep(1); \
;     if ((++_sp & 255u) == 0u) { if (xb_ld(&(bar)[XB_TMO])) break; if (_sp > XB_SPIN_CAP) { atomicAdd(&(bar)[XB_TMO], 1u); break; } } } } while (0)
;     __device__ __forceinline__ const float* x() const { return (const float*)ld(0); }
; __device__ __forceinline__ void xcd_barrier(const XcdBarrier& b) {
;     ...
;         } else {
;             XB_SPIN(xb_ld(&bar[XB_XGEN(b.x)]) == gen, bar);
;             asm volatile("buffer_inv sc0\n\ts_waitcnt vmcnt(0)" ::: "memory");
.LBB0_198:
	s_or_b64 exec, exec, s[8:9]
	s_waitcnt vmcnt(0)

; __device__ __forceinline__ unsigned xb_ld(unsigned* p)              { return __hip_atomic_load(p, __ATOMIC_RELAXED, __HIP_MEMORY_SCOPE_AGENT); }
; __device__ __forceinline__ unsigned xb_add(unsigned* p, unsigned v) { return __hip_atomic_fetch_add(p, v, __ATOMIC_RELAXED, __HIP_MEMORY_SCOPE_AGENT); }
; #define XB_SPIN(cond, bar) do { unsigned _sp = 0; while (cond) { __builtin_amdgcn_s_sleep(1); \
;     if ((++_sp & 255u) == 0u) { if (xb_ld(&(bar)[XB_TMO])) break; if (_sp > XB_SPIN_CAP) { atomicAdd(&(bar)[XB_TMO], 1u); break; } } } } while (0)
;     __device__ __forceinline__ const float* x() const { return (const float*)ld(0); }
; __device__ __forceinline__ void xcd_barrier(const XcdBarrier& b) {
;     ...
;         const unsigned old = xb_add(&bar[XB_XSUB(b.x)], 1u);
;         const unsigned gen = old / nloc;
;         if (old + 1u == (gen + 1u) * nloc) {
;             __builtin_amdgcn_fence(__ATOMIC_RELEASE, "agent");
;             asm volatile("s_waitcnt vmcnt(0)" ::: "memory");
;             const unsigned og = xb_add(&bar[XB_TOP], 1u);
;             const unsigned tg = og / nx;
;             if (og + 1u == (tg + 1u) * nx) xb_add(&bar[XB_TOPGEN], 1u);
;             else XB_SPIN(xb_ld(&bar[XB_TOPGEN]) == tg, bar);
.LBB0_202:
	s_or_b64 exec, exec, s[8:9]
	buffer_inv sc1
	v_cvt_f32_u32_e32 v4, v1
	s_waitcnt vmcnt(0)
	v_readfirstlane_b32 s2, v3
	s_add_u32 s8, s92, 0x3500
	s_addc_u32 s9, s93, 0
	v_rcp_iflag_f32_e32 v4, v4
	v_add_u32_e32 v2, s2, v2
	v_add_u32_e32 v5, 1, v2
	s_mov_b64 s[10:11], -1
	v_mul_f32_e32 v3, 0x4f7ffffe, v4
	v_cvt_u32_f32_e32 v3, v3
	v_sub_u32_e32 v4, 0, v1
	v_mul_lo_u32 v4, v4, v3
	v_mul_hi_u32 v4, v3, v4
	v_add_u32_e32 v3, v3, v4
	v_mul_hi_u32 v3, v2, v3
	v_mul_lo_u32 v4, v3, v1
	v_sub_u32_e32 v2, v2, v4
	v_add_u32_e32 v6, 1, v3
	v_cmp_ge_u32_e32 vcc, v2, v1
	v_sub_u32_e32 v4, v2, v1
	s_nop 0
	v_cndmask_b32_e32 v3, v3, v6, vcc
	v_cndmask_b32_e32 v2, v2, v4, vcc
	v_add_u32_e32 v4, 1, v3
	v_cmp_ge_u32_e32 vcc, v2, v1
	s_nop 1
	v_cndmask_b32_e32 v4, v3, v4, vcc
	v_mul_lo_u32 v2, v1, v4
	v_add_u32_e32 v1, v2, v1
	v_cmp_ne_u32_e32 vcc, v5, v1
	v_mov_b64_e32 v[2:3], s[8:9]
	s_and_saveexec_b64 s[2:3], vcc
	s_cbranch_execz .LBB0_216
	v_mov_b32_e32 v1, 0
	global_load_dword v2, v1, s[8:9] sc1
	s_mov_b64 s[14:15], 0
	s_waitcnt vmcnt(0)
	v_cmp_eq_u32_e32 vcc, v2, v4
	s_and_saveexec_b64 s[12:13], vcc
	s_cbranch_execz .LBB0_215
	s_add_u32 s10, s92, 0x200
	s_addc_u32 s11, s93, 0
	s_mov_b32 s24, 1
	s_branch .LBB0_206

; __device__ __forceinline__ unsigned xb_add(unsigned* p, unsigned v) { return __hip_atomic_fetch_add(p, v, __ATOMIC_RELAXED, __HIP_MEMORY_SCOPE_AGENT); }
;     __device__ __forceinline__ const float* x() const { return (const float*)ld(0); }
; __device__ __forceinline__ void xcd_barrier(const XcdBarrier& b) {
;     ...
;             __builtin_amdgcn_fence(__ATOMIC_ACQUIRE, "agent");
;             asm volatile("s_waitcnt vmcnt(0)" ::: "memory");
;             xb_add(&bar[XB_XGEN(b.x)], 1u);
;             asm volatile("s_waitcnt vmcnt(0)" ::: "memory");
.LBB0_218:
	s_or_b64 exec, exec, s[2:3]
	s_waitcnt vmcnt(0)
	s_waitcnt vmcnt(0)
	v_mov_b32_e32 v1, 0x2000
	v_mov_b32_e32 v2, 1
	global_atomic_add v1, v2, s[6:7] offset:1024

; __device__ __forceinline__ unsigned xb_ld(unsigned* p)              { return __hip_atomic_load(p, __ATOMIC_RELAXED, __HIP_MEMORY_SCOPE_AGENT); }
; __device__ __forceinline__ unsigned xb_add(unsigned* p, unsigned v) { return __hip_atomic_fetch_add(p, v, __ATOMIC_RELAXED, __HIP_MEMORY_SCOPE_AGENT); }
; #define XB_SPIN(cond, bar) do { unsigned _sp = 0; while (cond) { __builtin_amdgcn_s_sleep(1); \
;     if ((++_sp & 255u) == 0u) { if (xb_ld(&(bar)[XB_TMO])) break; if (_sp > XB_SPIN_CAP) { atomicAdd(&(bar)[XB_TMO], 1u); break; } } } } while (0)
;     __device__ __forceinline__ const float* x() const { return (const float*)ld(0); }
; __device__ __forceinline__ void xcd_barrier(const XcdBarrier& b) {
;     ...
;     if (threadIdx.x == 0) {
;         unsigned* bar = b.bar;
;         __builtin_amdgcn_s_waitcnt(0);
;         unsigned nloc = b.st[0], nx = b.st[1];
;         if (nloc == 0u) { xcd_barrier_complete(bar, b.x, nloc, nx); b.st[0] = nloc; b.st[1] = nx; }
;         const unsigned old = xb_add(&bar[XB_XSUB(b.x)], 1u);
;         const unsigned gen = old / nloc;
;         if (old + 1u == (gen + 1u) * nloc) {
;             __builtin_amdgcn_fence(__ATOMIC_RELEASE, "agent");
;             asm volatile("s_waitcnt vmcnt(0)" ::: "memory");
;             const unsigned og = xb_add(&bar[XB_TOP], 1u);
;             const unsigned tg = og / nx;
;             if (og + 1u == (tg + 1u) * nx) xb_add(&bar[XB_TOPGEN], 1u);
;             else XB_SPIN(xb_ld(&bar[XB_TOPGEN]) == tg, bar);
;             __builtin_amdgcn_fence(__ATOMIC_ACQUIRE, "agent");
;             asm volatile("s_waitcnt vmcnt(0)" ::: "memory");
;             xb_add(&bar[XB_XGEN(b.x)], 1u);
;             asm volatile("s_waitcnt vmcnt(0)" ::: "memory");
;         } else {
;             XB_SPIN(xb_ld(&bar[XB_XGEN(b.x)]) == gen, bar);
;             asm volatile("buffer_inv sc0\n\ts_waitcnt vmcnt(0)" ::: "memory");
.LBB0_610:
	v_readlane_b32 s2, v248, 2
	s_lshl_b32 s2, s2, 8
	s_add_u32 s8, s92, s2
	s_addc_u32 s9, s93, 0
	v_mov_b32_e32 v2, 0x1000
	v_mov_b32_e32 v4, 1
	global_atomic_add v4, v2, v4, s[8:9] offset:1024 sc0
	v_cvt_f32_u32_e32 v2, v3
	v_sub_u32_e32 v5, 0, v3
	v_rcp_iflag_f32_e32 v2, v2
	s_nop 0
	v_mul_f32_e32 v2, 0x4f7ffffe, v2
	v_cvt_u32_f32_e32 v2, v2
	v_mul_lo_u32 v5, v5, v2
	v_mul_hi_u32 v5, v2, v5
	v_add_u32_e32 v2, v2, v5
	s_waitcnt vmcnt(0)
	v_mul_hi_u32 v2, v4, v2
	v_mul_lo_u32 v5, v2, v3
	v_sub_u32_e32 v5, v4, v5
	v_add_u32_e32 v6, 1, v2
	v_cmp_ge_u32_e32 vcc, v5, v3
	v_add_u32_e32 v4, 1, v4
	s_nop 0
	v_cndmask_b32_e32 v2, v2, v6, vcc
	v_sub_u32_e32 v6, v5, v3
	v_cndmask_b32_e32 v5, v5, v6, vcc
	v_add_u32_e32 v6, 1, v2
	v_cmp_ge_u32_e32 vcc, v5, v3
	s_nop 1
	v_cndmask_b32_e32 v2, v2, v6, vcc
	v_mul_lo_u32 v5, v3, v2
	v_add_u32_e32 v3, v5, v3
	v_cmp_ne_u32_e32 vcc, v4, v3
	s_and_saveexec_b64 s[2:3], vcc
	s_xor_b64 s[2:3], exec, s[2:3]
	s_cbranch_execz .LBB0_624
	s_waitcnt lgkmcnt(0)
	buffer_inv sc0
	v_mov_b32_e32 v1, 0x2000
	global_load_dword v1, v1, s[8:9] offset:1024 sc1
	s_add_u32 s12, s8, 0x2400
	s_addc_u32 s13, s9, 0
	s_waitcnt vmcnt(0)
	v_cmp_eq_u32_e32 vcc, v1, v2
	s_and_saveexec_b64 s[10:11], vcc
	s_cbranch_execz .LBB0_623
	s_mov_b32 s24, 1
	s_mov_b64 s[14:15], 0
	v_mov_b32_e32 v1, 0
	s_branch .LBB0_614

; __device__ __forceinline__ unsigned xb_ld(unsigned* p)              { return __hip_atomic_load(p, __ATOMIC_RELAXED, __HIP_MEMORY_SCOPE_AGENT); }
; #define XB_SPIN(cond, bar) do { unsigned _sp = 0; while (cond) { __builtin_amdgcn_s_sleep(1); \
;     if ((++_sp & 255u) == 0u) { if (xb_ld(&(bar)[XB_TMO])) break; if (_sp > XB_SPIN_CAP) { atomicAdd(&(bar)[XB_TMO], 1u); break; } } } } while (0)
;     __device__ __forceinline__ const float* x() const { return (const float*)ld(0); }
; __device__ __forceinline__ void xcd_barrier(const XcdBarrier& b) {
;     ...
;         } else {
;             XB_SPIN(xb_ld(&bar[XB_XGEN(b.x)]) == gen, bar);
;             asm volatile("buffer_inv sc0\n\ts_waitcnt vmcnt(0)" ::: "memory");
.LBB0_623:
	s_or_b64 exec, exec, s[10:11]
	s_waitcnt vmcnt(0)

; __device__ __forceinline__ unsigned xb_ld(unsigned* p)              { return __hip_atomic_load(p, __ATOMIC_RELAXED, __HIP_MEMORY_SCOPE_AGENT); }
; __device__ __forceinline__ unsigned xb_add(unsigned* p, unsigned v) { return __hip_atomic_fetch_add(p, v, __ATOMIC_RELAXED, __HIP_MEMORY_SCOPE_AGENT); }
; #define XB_SPIN(cond, bar) do { unsigned _sp = 0; while (cond) { __builtin_amdgcn_s_sleep(1); \
;     if ((++_sp & 255u) == 0u) { if (xb_ld(&(bar)[XB_TMO])) break; if (_sp > XB_SPIN_CAP) { atomicAdd(&(bar)[XB_TMO], 1u); break; } } } } while (0)
;     __device__ __forceinline__ const float* x() const { return (const float*)ld(0); }
; __device__ __forceinline__ void xcd_barrier(const XcdBarrier& b) {
;     ...
;         const unsigned old = xb_add(&bar[XB_XSUB(b.x)], 1u);
;         const unsigned gen = old / nloc;
;         if (old + 1u == (gen + 1u) * nloc) {
;             __builtin_amdgcn_fence(__ATOMIC_RELEASE, "agent");
;             asm volatile("s_waitcnt vmcnt(0)" ::: "memory");
;             const unsigned og = xb_add(&bar[XB_TOP], 1u);
;             const unsigned tg = og / nx;
;             if (og + 1u == (tg + 1u) * nx) xb_add(&bar[XB_TOPGEN], 1u);
;             else XB_SPIN(xb_ld(&bar[XB_TOPGEN]) == tg, bar);
.LBB0_627:
	s_or_b64 exec, exec, s[10:11]
	buffer_inv sc1
	v_cvt_f32_u32_e32 v4, v1
	s_waitcnt vmcnt(0)
	v_readfirstlane_b32 s2, v3
	s_add_u32 s10, s92, 0x3500
	s_addc_u32 s11, s93, 0
	v_rcp_iflag_f32_e32 v4, v4
	v_add_u32_e32 v2, s2, v2
	v_add_u32_e32 v5, 1, v2
	s_mov_b64 s[12:13], -1
	v_mul_f32_e32 v3, 0x4f7ffffe, v4
	v_cvt_u32_f32_e32 v3, v3
	v_sub_u32_e32 v4, 0, v1
	v_mul_lo_u32 v4, v4, v3
	v_mul_hi_u32 v4, v3, v4
	v_add_u32_e32 v3, v3, v4
	v_mul_hi_u32 v3, v2, v3
	v_mul_lo_u32 v4, v3, v1
	v_sub_u32_e32 v2, v2, v4
	v_add_u32_e32 v6, 1, v3
	v_cmp_ge_u32_e32 vcc, v2, v1
	v_sub_u32_e32 v4, v2, v1
	s_nop 0
	v_cndmask_b32_e32 v3, v3, v6, vcc
	v_cndmask_b32_e32 v2, v2, v4, vcc
	v_add_u32_e32 v4, 1, v3
	v_cmp_ge_u32_e32 vcc, v2, v1
	s_nop 1
	v_cndmask_b32_e32 v4, v3, v4, vcc
	v_mul_lo_u32 v2, v1, v4
	v_add_u32_e32 v1, v2, v1
	v_cmp_ne_u32_e32 vcc, v5, v1
	v_mov_b64_e32 v[2:3], s[10:11]
	s_and_saveexec_b64 s[2:3], vcc
	s_cbranch_execz .LBB0_639
	v_mov_b32_e32 v1, 0
	global_load_dword v2, v1, s[10:11] sc1
	s_mov_b64 s[16:17], 0
	s_waitcnt vmcnt(0)
	v_cmp_eq_u32_e32 vcc, v2, v4
	s_and_saveexec_b64 s[14:15], vcc
	s_cbranch_execz .LBB0_638
	s_add_u32 s12, s92, 0x200
	s_addc_u32 s13, s93, 0
	s_mov_b32 s26, 1
	s_branch .LBB0_631

; __device__ __forceinline__ unsigned xb_add(unsigned* p, unsigned v) { return __hip_atomic_fetch_add(p, v, __ATOMIC_RELAXED, __HIP_MEMORY_SCOPE_AGENT); }
;     __device__ __forceinline__ const float* x() const { return (const float*)ld(0); }
; __device__ __forceinline__ void xcd_barrier(const XcdBarrier& b) {
;     ...
;             __builtin_amdgcn_fence(__ATOMIC_ACQUIRE, "agent");
;             asm volatile("s_waitcnt vmcnt(0)" ::: "memory");
;             xb_add(&bar[XB_XGEN(b.x)], 1u);
;             asm volatile("s_waitcnt vmcnt(0)" ::: "memory");
.LBB0_641:
	s_or_b64 exec, exec, s[2:3]
	s_waitcnt vmcnt(0)
	s_waitcnt vmcnt(0)
	v_mov_b32_e32 v1, 0x2000
	v_mov_b32_e32 v2, 1
	global_atomic_add v1, v2, s[8:9] offset:1024
